# P5 ml_out: one throw-away LDS-DMA load per wave prefetches the next item's K fragments and C_in blocks into L2
# baseline (speedup 1.0000x reference)
.LBB0_975:
	v_or_b32_e32 v37, s82, v153
	v_readlane_b32 s52, v254, 57
	v_add_u32_e32 v42, s81, v217
	v_lshlrev_b32_e32 v154, 1, v37
	v_readlane_b32 s53, v254, 58
	v_or_b32_e32 v40, 1, v42
	v_or_b32_e32 v38, 2, v42
	v_lshl_add_u64 v[26:27], s[52:53], 0, v[154:155]
	v_or_b32_e32 v36, 3, v42
	v_or_b32_e32 v41, 16, v37
	v_mov_b64_e32 v[34:35], s[52:53]
	v_mad_i64_i32 v[28:29], s[50:51], v42, s80, v[26:27]
	v_mad_i64_i32 v[30:31], s[50:51], v40, s80, v[26:27]
	v_mad_i64_i32 v[32:33], s[50:51], v38, s80, v[26:27]
	v_mad_i64_i32 v[26:27], s[50:51], v36, s80, v[26:27]
	v_mad_i64_i32 v[58:59], s[50:51], v42, s80, v[34:35]
	v_lshlrev_b32_e32 v46, 1, v41
	v_mov_b32_e32 v47, v155
	v_mad_i64_i32 v[82:83], s[50:51], v40, s80, v[34:35]
	v_mad_i64_i32 v[84:85], s[50:51], v38, s80, v[34:35]
	v_mad_i64_i32 v[86:87], s[50:51], v36, s80, v[34:35]
	v_lshl_add_u64 v[44:45], v[58:59], 0, v[46:47]
	v_lshl_add_u64 v[54:55], v[82:83], 0, v[46:47]
	v_lshl_add_u64 v[56:57], v[84:85], 0, v[46:47]
	v_lshl_add_u64 v[34:35], v[86:87], 0, v[46:47]
	global_load_ushort v50, v[28:29], off
	global_load_ushort v49, v[30:31], off
	global_load_ushort v48, v[32:33], off
	global_load_ushort v51, v[26:27], off
	global_load_ushort v52, v[44:45], off
	global_load_ushort v53, v[54:55], off
	global_load_ushort v61, v[56:57], off
	global_load_ushort v63, v[34:35], off
	v_or_b32_e32 v26, 32, v37
	v_lshlrev_b32_e32 v44, 1, v26
	v_mov_b32_e32 v45, v155
	v_or_b32_e32 v34, 48, v37
	v_lshl_add_u64 v[26:27], v[58:59], 0, v[44:45]
	v_lshl_add_u64 v[30:31], v[84:85], 0, v[44:45]
	v_lshlrev_b32_e32 v34, 1, v34
	v_mov_b32_e32 v35, v155
	v_lshl_add_u64 v[28:29], v[82:83], 0, v[44:45]
	v_lshl_add_u64 v[32:33], v[86:87], 0, v[44:45]
	v_lshl_add_u64 v[54:55], v[58:59], 0, v[34:35]
	v_lshl_add_u64 v[56:57], v[82:83], 0, v[34:35]
	v_lshl_add_u64 v[68:69], v[84:85], 0, v[34:35]
	v_lshl_add_u64 v[70:71], v[86:87], 0, v[34:35]
	global_load_ushort v64, v[26:27], off
	global_load_ushort v66, v[28:29], off
	global_load_ushort v80, v[30:31], off
	global_load_ushort v79, v[32:33], off
	global_load_ushort v78, v[54:55], off
	global_load_ushort v77, v[56:57], off
	global_load_ushort v76, v[68:69], off
	global_load_ushort v75, v[70:71], off
	v_or_b32_e32 v26, 64, v37
	v_or_b32_e32 v30, 0x50, v37
	v_lshlrev_b32_e32 v32, 1, v26
	v_mov_b32_e32 v33, v155
	v_lshlrev_b32_e32 v30, 1, v30
	v_mov_b32_e32 v31, v155
	v_lshl_add_u64 v[26:27], v[58:59], 0, v[32:33]
	v_lshl_add_u64 v[68:69], v[58:59], 0, v[30:31]
	v_lshl_add_u64 v[28:29], v[82:83], 0, v[32:33]
	v_lshl_add_u64 v[54:55], v[84:85], 0, v[32:33]
	v_lshl_add_u64 v[56:57], v[86:87], 0, v[32:33]
	v_lshl_add_u64 v[88:89], v[82:83], 0, v[30:31]
	v_lshl_add_u64 v[90:91], v[84:85], 0, v[30:31]
	v_lshl_add_u64 v[92:93], v[86:87], 0, v[30:31]
	global_load_ushort v74, v[26:27], off
	global_load_ushort v73, v[28:29], off
	global_load_ushort v72, v[54:55], off
	global_load_ushort v71, v[56:57], off
	global_load_ushort v70, v[68:69], off
	s_nop 0
	global_load_ushort v69, v[88:89], off
	global_load_ushort v68, v[90:91], off
	global_load_ushort v67, v[92:93], off
	v_or_b32_e32 v26, 0x60, v37
	v_lshlrev_b32_e32 v28, 1, v26
	v_mov_b32_e32 v29, v155
	v_or_b32_e32 v26, 0x70, v37
	v_readlane_b32 s76, v252, 25
	v_lshlrev_b32_e32 v39, 2, v37
	v_lshl_add_u64 v[88:89], v[58:59], 0, v[28:29]
	v_readlane_b32 s88, v252, 37
	v_readlane_b32 s89, v252, 38
	v_lshlrev_b32_e32 v26, 1, v26
	v_mov_b32_e32 v27, v155
	v_lshl_add_u64 v[90:91], v[82:83], 0, v[28:29]
	v_lshl_add_u64 v[92:93], v[84:85], 0, v[28:29]
	v_lshl_add_u64 v[94:95], v[86:87], 0, v[28:29]
	global_load_dword v47, v39, s[88:89]
	global_load_dword v45, v39, s[88:89] offset:64
	global_load_dword v35, v39, s[88:89] offset:128
	global_load_dword v33, v39, s[88:89] offset:192
	global_load_dword v31, v39, s[88:89] offset:256
	global_load_dword v29, v39, s[88:89] offset:320
	global_load_dword v57, v39, s[88:89] offset:384
	global_load_dword v54, v39, s[88:89] offset:448
	v_lshl_add_u64 v[96:97], v[58:59], 0, v[26:27]
	v_lshl_add_u64 v[82:83], v[82:83], 0, v[26:27]
	v_lshl_add_u64 v[84:85], v[84:85], 0, v[26:27]
	v_lshl_add_u64 v[86:87], v[86:87], 0, v[26:27]
	global_load_ushort v65, v[88:89], off
	global_load_ushort v62, v[90:91], off
	global_load_ushort v60, v[92:93], off
	global_load_ushort v59, v[94:95], off
	global_load_ushort v27, v[96:97], off
	global_load_ushort v58, v[82:83], off
	global_load_ushort v56, v[84:85], off
	global_load_ushort v55, v[86:87], off
	v_readlane_b32 s50, v253, 12
	v_readlane_b32 s33, v255, 2
	s_add_i32 s33, s33, s50
	s_cmpk_gt_i32 s33, 0x3ff
	s_cselect_b64 s[52:53], -1, 0
	s_cmpk_lt_i32 s33, 0x400
	v_writelane_b32 v255, s33, 2
	s_cselect_b32 s33, s33, -1
	s_movk_i32 s56, 0x3200
	s_cmp_gt_i32 s33, -1
	v_readlane_b32 s77, v252, 26
	v_readlane_b32 s78, v252, 27
	v_readlane_b32 s79, v252, 28
	v_readlane_b32 s80, v252, 29
	v_readlane_b32 s81, v252, 30
	v_readlane_b32 s82, v252, 31
	v_readlane_b32 s83, v252, 32
	v_readlane_b32 s84, v252, 33
	v_readlane_b32 s85, v252, 34
	v_readlane_b32 s86, v252, 35
	v_readlane_b32 s87, v252, 36
	v_readlane_b32 s90, v252, 39
	v_readlane_b32 s91, v252, 40
	v_readlane_b32 s51, v253, 13
	s_cbranch_scc0 .LBB0_837
	s_and_b32 s54, s33, 7
	s_lshl_b32 s33, s33, 4
	s_and_b32 s33, s33, 0x7fffff80
	s_lshl_b32 s50, s54, 14
	s_add_i32 s50, s50, s33
	s_mov_b32 s51, s60
	s_lshl_b64 s[50:51], s[50:51], 7
	v_readlane_b32 s55, v253, 34
	v_mov_b32_e32 v1, v206
	s_add_u32 s50, s55, s50
	v_readlane_b32 s55, v253, 35
	s_addc_u32 s51, s55, s51
	v_readlane_b32 s55, v253, 33
	v_readlane_b32 s76, v252, 2
	v_mov_b32_e32 v3, v155
	v_and_or_b32 v2, v1, 15, s55
	v_ashrrev_i32_e32 v1, 1, v1
	v_and_b32_e32 v4, -8, v1
	v_lshrrev_b32_e32 v1, 2, v0
	v_readlane_b32 s78, v252, 4
	v_readlane_b32 s79, v252, 5
	v_lshlrev_b64 v[2:3], 7, v[2:3]
	v_or_b32_e32 v1, s33, v1
	v_mov_b64_e32 v[10:11], s[78:79]
	v_lshl_add_u64 v[2:3], s[50:51], 0, v[2:3]
	v_mad_u64_u32 v[10:11], s[50:51], v1, s56, v[10:11]
	s_lshl_b32 s50, s54, 8
	s_mov_b32 s51, s60
	v_lshl_add_u64 v[10:11], v[10:11], 0, s[50:51]
	v_mov_b32_e32 v151, v155
	v_lshl_add_u64 v[10:11], v[10:11], 0, v[150:151]
	s_mov_b64 s[50:51], 0x1eb00400
	s_mov_b32 s33, 0x1eb00000
	v_ashrrev_i32_e32 v5, 31, v4
	v_lshl_add_u64 v[22:23], v[10:11], 0, s[50:51]
	v_add_co_u32_e32 v10, vcc, s33, v10
	v_lshl_add_u64 v[6:7], v[4:5], 1, v[2:3]
	s_nop 0
	v_addc_co_u32_e32 v11, vcc, 0, v11, vcc
	global_load_dwordx4 v[2:5], v[6:7], off
	s_nop 0
	global_load_dwordx4 v[6:9], v[6:7], off offset:64
	s_nop 0
	global_load_dwordx4 v[14:17], v[22:23], off offset:16
	global_load_dwordx4 v[18:21], v[22:23], off offset:32
	s_nop 0
	global_load_dwordx4 v[10:13], v[10:11], off offset:1024
	s_nop 0
	global_load_dwordx4 v[22:25], v[22:23], off offset:48
	v_readlane_b32 s100, v255, 2
	v_readfirstlane_b32 s101, v0
	s_lshr_b32 s101, s101, 6
	s_and_b32 s32, s100, 7
	s_lshl_b32 s32, s32, 21
	s_lshr_b32 s100, s100, 3
	s_lshl_b32 s100, s100, 14
	s_add_u32 s32, s32, s100
	s_and_b32 s100, s101, 1
	s_lshl_b32 s100, s100, 13
	s_add_u32 s32, s32, s100
	s_lshr_b32 s101, s101, 1
	s_mov_b32 s100, 0x3e700000
	s_cmp_eq_u32 s101, 1
	s_cselect_b32 s98, 0x3000000, 0
	s_sub_u32 s100, s100, s98
	s_cmp_eq_u32 s101, 2
	s_cselect_b32 s98, 0x2000000, 0
	s_sub_u32 s100, s100, s98
	s_add_u32 s32, s32, s100
	s_add_u32 s98, s78, s32
	s_addc_u32 s99, s79, 0
	s_mov_b32 m0, 0x24c00
	v_lshlrev_b32_e32 v1, 7, v206
	global_load_lds_dword v1, s[98:99]
	v_readlane_b32 s77, v252, 3
	s_branch .LBB0_837
